# up-projection output: half of H (rows 128-255 of each tile) stored with the default cache policy, the other half nt
# speedup vs baseline: 1.0175x; 1.0115x over previous
; #define PG8_LAS __attribute__((address_space(3)))
; #define PG8_GAS __attribute__((address_space(1)))
; #define PG8_PACK8(y0, y1) (u32x4){cvt_pk_bf16((y0)[0], (y0)[1]), cvt_pk_bf16((y0)[2], (y0)[3]), cvt_pk_bf16((y1)[0], (y1)[1]), cvt_pk_bf16((y1)[2], (y1)[3])}
;     __device__ __forceinline__ void operator()(const f32x4 (&acc)[2][2][4][2], const Unit& u, int ui, int wr, int wc, int fr, int fq) const {
;     ...
;         const unsigned row0 = (unsigned)(u.pm * BM + wr * 64 + fr), colp = (unsigned)((u.pn & 3) * BM + wc * 32 + 8 * fq);
;         const PG8_LAS float* rsp = tab + (u.pm == pmA ? 0 : 256) + wr * 64 + fr;
;         float rsv[2][4];
; #pragma unroll
;         for (int ai = 0; ai < 2; ++ai)
; #pragma unroll
;             for (int m = 0; m < 4; ++m) rsv[ai][m] = rsp[ai * HALF + m * 16];
; #pragma unroll
;         for (int ai = 0; ai < 2; ++ai)
; #pragma unroll
;             for (int m = 0; m < 4; ++m) {
;                 const unsigned row = row0 + ai * HALF + m * 16; const float rs = rsv[ai][m];
; #pragma unroll
;                 for (int bj = 0; bj < 2; ++bj) {
;                     f32x4 y0 = acc[ai][bj][m][0] * rs, y1 = acc[ai][bj][m][1] * rs;
; #pragma unroll
;                     for (int e = 0; e < 4; ++e) { const float a = fmaxf(y0[e], 0.f), b = fmaxf(y1[e], 0.f); y0[e] = a * a; y1[e] = b * b; }
;                     const u32x4 hw = PG8_PACK8(y0, y1);
;     ...
;                     if (probe_mode == 1) { asm volatile("" :: "v"(hw)); } else
;     ...
;                     *(PG8_GAS u32x4*)((PG8_GAS unsigned char*)ws + E_QKVO + (size_t)((unsigned)(u.pm >> 4) * (24u << 20) + (unsigned)(u.pn >> 2) * (8u << 20) + row * 2048u + (colp + bj * HALF) * 2u)) = hw;
;                 }
.LBB0_64:
	s_lshl_b32 s13, s51, 9
	s_cmp_eq_u32 s20, s29
	s_cselect_b32 s15, 0, 0x400
	v_add_u32_e32 v140, s15, v145
	ds_read2_b32 v[164:165], v140 offset1:16
	ds_read2_b32 v[166:167], v140 offset0:32 offset1:48
	ds_read2_b32 v[142:143], v140 offset0:128 offset1:144
	ds_read2_b32 v[140:141], v140 offset0:160 offset1:176
	s_lshl_b32 s22, s51, 21
	s_lshr_b32 s15, s20, 4
	s_and_b32 s22, s22, 0xff800000
	s_lshl_b32 s20, s20, 19
	s_waitcnt lgkmcnt(0)
	v_pk_mul_f32 v[122:123], v[122:123], v[164:165] op_sel_hi:[1,0]
	s_add_i32 s22, s22, s20
	v_pk_mul_f32 v[126:127], v[126:127], v[164:165] op_sel_hi:[1,0]
	v_pk_mul_f32 v[124:125], v[124:125], v[164:165] op_sel_hi:[1,0]
	v_max_f32_e32 v122, 0, v122
	s_and_b32 s13, s13, 0x600
	v_add_u32_e32 v163, s22, v146
	v_pk_mul_f32 v[128:129], v[128:129], v[164:165] op_sel_hi:[1,0]
	v_mul_f32_e32 v168, v122, v122
	v_max_f32_e32 v122, 0, v127
	v_max_f32_e32 v123, 0, v123
	v_max_f32_e32 v124, 0, v124
	s_mul_i32 s15, s15, 0x1800000
	v_or_b32_e32 v163, s13, v163
	v_max_f32_e32 v126, 0, v126
	v_mul_f32_e32 v122, v122, v122
	v_mul_f32_e32 v127, v123, v123
	v_max_f32_e32 v123, 0, v128
	v_mul_f32_e32 v128, v124, v124
	v_max_f32_e32 v124, 0, v129
	v_max_f32_e32 v125, 0, v125
	v_pk_mul_f32 v[114:115], v[114:115], v[164:165] op_sel_hi:[1,0]
	v_add_u32_e32 v163, s15, v163
	v_mul_f32_e32 v126, v126, v126
	v_mul_f32_e32 v123, v123, v123
	v_mul_f32_e32 v124, v124, v124
	v_mul_f32_e32 v125, v125, v125
	v_cvt_pk_bf16_f32 v122, v126, v122
	v_pk_mul_f32 v[120:121], v[120:121], v[164:165] op_sel_hi:[1,0]
	v_pk_mul_f32 v[118:119], v[118:119], v[164:165] op_sel_hi:[1,0]
	v_pk_mul_f32 v[116:117], v[116:117], v[164:165] op_sel_hi:[1,0]
	v_max_f32_e32 v114, 0, v114
	v_max_f32_e32 v115, 0, v115
	v_cvt_pk_bf16_f32 v123, v123, v124
	v_cvt_pk_bf16_f32 v124, v168, v127
	v_cvt_pk_bf16_f32 v125, v128, v125
	global_store_dwordx4 v163, v[122:125], s[10:11] nt
	v_max_f32_e32 v118, 0, v118
	v_max_f32_e32 v116, 0, v116
	v_mul_f32_e32 v122, v114, v114
	v_max_f32_e32 v114, 0, v119
	v_mul_f32_e32 v119, v115, v115
	v_max_f32_e32 v115, 0, v120
	v_mul_f32_e32 v118, v118, v118
	v_mul_f32_e32 v114, v114, v114
	v_mul_f32_e32 v115, v115, v115
	v_mul_f32_e32 v120, v116, v116
	v_max_f32_e32 v116, 0, v121
	v_max_f32_e32 v117, 0, v117
	v_mul_f32_e32 v116, v116, v116
	v_mul_f32_e32 v117, v117, v117
	v_cvt_pk_bf16_f32 v114, v118, v114
	v_cvt_pk_bf16_f32 v115, v115, v116
	v_or_b32_e32 v118, 0x100, v163
	v_cvt_pk_bf16_f32 v116, v122, v119
	v_cvt_pk_bf16_f32 v117, v120, v117
	global_store_dwordx4 v118, v[114:117], s[10:11] nt
	v_pk_mul_f32 v[90:91], v[90:91], v[166:167] op_sel_hi:[1,0]
	v_pk_mul_f32 v[94:95], v[94:95], v[166:167] op_sel_hi:[1,0]
	v_or_b32_e32 v115, 0x8000, v163
	v_mov_b32_e32 v114, v165
	v_pk_mul_f32 v[106:107], v[106:107], v[114:115] op_sel_hi:[1,0]
	v_pk_mul_f32 v[110:111], v[110:111], v[114:115] op_sel_hi:[1,0]
	v_pk_mul_f32 v[108:109], v[108:109], v[114:115] op_sel_hi:[1,0]
	v_max_f32_e32 v106, 0, v106
	v_pk_mul_f32 v[112:113], v[112:113], v[114:115] op_sel_hi:[1,0]
	v_mul_f32_e32 v116, v106, v106
	v_max_f32_e32 v106, 0, v111
	v_max_f32_e32 v107, 0, v107
	v_max_f32_e32 v108, 0, v108
	v_max_f32_e32 v110, 0, v110
	v_mul_f32_e32 v106, v106, v106
	v_mul_f32_e32 v111, v107, v107
	v_max_f32_e32 v107, 0, v112
	v_mul_f32_e32 v112, v108, v108
	v_max_f32_e32 v108, 0, v113
	v_max_f32_e32 v109, 0, v109
	v_pk_mul_f32 v[98:99], v[98:99], v[114:115] op_sel_hi:[1,0]
	v_mul_f32_e32 v110, v110, v110
	v_mul_f32_e32 v107, v107, v107
	v_mul_f32_e32 v108, v108, v108
	v_mul_f32_e32 v109, v109, v109
	v_cvt_pk_bf16_f32 v106, v110, v106
	v_pk_mul_f32 v[104:105], v[104:105], v[114:115] op_sel_hi:[1,0]
	v_pk_mul_f32 v[102:103], v[102:103], v[114:115] op_sel_hi:[1,0]
	v_pk_mul_f32 v[100:101], v[100:101], v[114:115] op_sel_hi:[1,0]
	v_max_f32_e32 v98, 0, v98
	v_max_f32_e32 v99, 0, v99
	v_cvt_pk_bf16_f32 v107, v107, v108
	v_cvt_pk_bf16_f32 v108, v116, v111
	v_cvt_pk_bf16_f32 v109, v112, v109
	global_store_dwordx4 v115, v[106:109], s[10:11] nt
	v_max_f32_e32 v102, 0, v102
	v_max_f32_e32 v100, 0, v100
	v_mul_f32_e32 v106, v98, v98
	v_max_f32_e32 v98, 0, v103
	v_mul_f32_e32 v103, v99, v99
	v_max_f32_e32 v99, 0, v104
	v_mul_f32_e32 v102, v102, v102
	v_mul_f32_e32 v98, v98, v98
	v_mul_f32_e32 v99, v99, v99
	v_mul_f32_e32 v104, v100, v100
	v_max_f32_e32 v100, 0, v105
	v_max_f32_e32 v101, 0, v101
	v_mul_f32_e32 v100, v100, v100
	v_mul_f32_e32 v101, v101, v101
	v_cvt_pk_bf16_f32 v98, v102, v98
	v_cvt_pk_bf16_f32 v99, v99, v100
	v_or_b32_e32 v102, 0x8100, v163
	v_pk_mul_f32 v[92:93], v[92:93], v[166:167] op_sel_hi:[1,0]
	v_max_f32_e32 v90, 0, v90
	v_cvt_pk_bf16_f32 v100, v106, v103
	v_cvt_pk_bf16_f32 v101, v104, v101
	global_store_dwordx4 v102, v[98:101], s[10:11] nt
	v_pk_mul_f32 v[96:97], v[96:97], v[166:167] op_sel_hi:[1,0]
	v_max_f32_e32 v91, 0, v91
	v_mul_f32_e32 v99, v90, v90
	v_max_f32_e32 v90, 0, v95
	v_max_f32_e32 v92, 0, v92
	v_max_f32_e32 v94, 0, v94
	v_mul_f32_e32 v90, v90, v90
	v_mul_f32_e32 v95, v91, v91
	v_max_f32_e32 v91, 0, v96
	v_mul_f32_e32 v96, v92, v92
	v_max_f32_e32 v92, 0, v97
	v_max_f32_e32 v93, 0, v93
	v_pk_mul_f32 v[82:83], v[82:83], v[166:167] op_sel_hi:[1,0]
	v_or_b32_e32 v98, 0x10000, v163
	v_mul_f32_e32 v94, v94, v94
	v_mul_f32_e32 v91, v91, v91
	v_mul_f32_e32 v92, v92, v92
	v_mul_f32_e32 v93, v93, v93
	v_cvt_pk_bf16_f32 v90, v94, v90
	v_pk_mul_f32 v[88:89], v[88:89], v[166:167] op_sel_hi:[1,0]
	v_pk_mul_f32 v[86:87], v[86:87], v[166:167] op_sel_hi:[1,0]
	v_pk_mul_f32 v[84:85], v[84:85], v[166:167] op_sel_hi:[1,0]
	v_max_f32_e32 v82, 0, v82
	v_max_f32_e32 v83, 0, v83
	v_cvt_pk_bf16_f32 v91, v91, v92
	v_cvt_pk_bf16_f32 v92, v99, v95
	v_cvt_pk_bf16_f32 v93, v96, v93
; #define PG8_GAS __attribute__((address_space(1)))
; #define PG8_PACK8(y0, y1) (u32x4){cvt_pk_bf16((y0)[0], (y0)[1]), cvt_pk_bf16((y0)[2], (y0)[3]), cvt_pk_bf16((y1)[0], (y1)[1]), cvt_pk_bf16((y1)[2], (y1)[3])}
;     __device__ __forceinline__ void operator()(const f32x4 (&acc)[2][2][4][2], const Unit& u, int ui, int wr, int wc, int fr, int fq) const {
;     ...
;         for (int ai = 0; ai < 2; ++ai)
; #pragma unroll
;             for (int m = 0; m < 4; ++m) {
;                 const unsigned row = row0 + ai * HALF + m * 16; const float rs = rsv[ai][m];
; #pragma unroll
;                 for (int bj = 0; bj < 2; ++bj) {
;                     f32x4 y0 = acc[ai][bj][m][0] * rs, y1 = acc[ai][bj][m][1] * rs;
; #pragma unroll
;                     for (int e = 0; e < 4; ++e) { const float a = fmaxf(y0[e], 0.f), b = fmaxf(y1[e], 0.f); y0[e] = a * a; y1[e] = b * b; }
;                     const u32x4 hw = PG8_PACK8(y0, y1);
;     ...
;                     if (probe_mode == 1) { asm volatile("" :: "v"(hw)); } else
;     ...
;                     *(PG8_GAS u32x4*)((PG8_GAS unsigned char*)ws + E_QKVO + (size_t)((unsigned)(u.pm >> 4) * (24u << 20) + (unsigned)(u.pn >> 2) * (8u << 20) + row * 2048u + (colp + bj * HALF) * 2u)) = hw;
;                 }
	global_store_dwordx4 v98, v[90:93], s[10:11] nt
	v_max_f32_e32 v86, 0, v86
	v_max_f32_e32 v84, 0, v84
	v_mul_f32_e32 v90, v82, v82
	v_max_f32_e32 v82, 0, v87
	v_mul_f32_e32 v87, v83, v83
	v_max_f32_e32 v83, 0, v88
	v_mul_f32_e32 v86, v86, v86
	v_mul_f32_e32 v82, v82, v82
	v_mul_f32_e32 v83, v83, v83
	v_mul_f32_e32 v88, v84, v84
	v_max_f32_e32 v84, 0, v89
	v_max_f32_e32 v85, 0, v85
	v_mul_f32_e32 v84, v84, v84
	v_mul_f32_e32 v85, v85, v85
	v_cvt_pk_bf16_f32 v82, v86, v82
	v_cvt_pk_bf16_f32 v83, v83, v84
	v_or_b32_e32 v86, 0x10100, v163
	v_cvt_pk_bf16_f32 v84, v90, v87
	v_cvt_pk_bf16_f32 v85, v88, v85
	global_store_dwordx4 v86, v[82:85], s[10:11] nt
	v_pk_mul_f32 v[58:59], v[58:59], v[142:143] op_sel_hi:[1,0]
	v_pk_mul_f32 v[62:63], v[62:63], v[142:143] op_sel_hi:[1,0]
	v_or_b32_e32 v83, 0x18000, v163
	v_mov_b32_e32 v82, v167
	v_pk_mul_f32 v[74:75], v[74:75], v[82:83] op_sel_hi:[1,0]
	v_pk_mul_f32 v[78:79], v[78:79], v[82:83] op_sel_hi:[1,0]
	v_pk_mul_f32 v[76:77], v[76:77], v[82:83] op_sel_hi:[1,0]
	v_max_f32_e32 v74, 0, v74
	v_pk_mul_f32 v[80:81], v[80:81], v[82:83] op_sel_hi:[1,0]
	v_mul_f32_e32 v84, v74, v74
	v_max_f32_e32 v74, 0, v79
	v_max_f32_e32 v75, 0, v75
	v_max_f32_e32 v76, 0, v76
	v_max_f32_e32 v78, 0, v78
	v_mul_f32_e32 v74, v74, v74
	v_mul_f32_e32 v79, v75, v75
	v_max_f32_e32 v75, 0, v80
	v_mul_f32_e32 v80, v76, v76
	v_max_f32_e32 v76, 0, v81
	v_max_f32_e32 v77, 0, v77
	v_pk_mul_f32 v[66:67], v[66:67], v[82:83] op_sel_hi:[1,0]
	v_mul_f32_e32 v78, v78, v78
	v_mul_f32_e32 v75, v75, v75
	v_mul_f32_e32 v76, v76, v76
	v_mul_f32_e32 v77, v77, v77
	v_cvt_pk_bf16_f32 v74, v78, v74
	v_pk_mul_f32 v[72:73], v[72:73], v[82:83] op_sel_hi:[1,0]
	v_pk_mul_f32 v[70:71], v[70:71], v[82:83] op_sel_hi:[1,0]
	v_pk_mul_f32 v[68:69], v[68:69], v[82:83] op_sel_hi:[1,0]
	v_max_f32_e32 v66, 0, v66
	v_max_f32_e32 v67, 0, v67
	v_cvt_pk_bf16_f32 v75, v75, v76
	v_cvt_pk_bf16_f32 v76, v84, v79
	v_cvt_pk_bf16_f32 v77, v80, v77
	global_store_dwordx4 v83, v[74:77], s[10:11] nt
	v_max_f32_e32 v70, 0, v70
	v_max_f32_e32 v68, 0, v68
	v_mul_f32_e32 v74, v66, v66
	v_max_f32_e32 v66, 0, v71
	v_mul_f32_e32 v71, v67, v67
	v_max_f32_e32 v67, 0, v72
	v_mul_f32_e32 v70, v70, v70
	v_mul_f32_e32 v66, v66, v66
	v_mul_f32_e32 v67, v67, v67
	v_mul_f32_e32 v72, v68, v68
	v_max_f32_e32 v68, 0, v73
	v_max_f32_e32 v69, 0, v69
	v_mul_f32_e32 v68, v68, v68
	v_mul_f32_e32 v69, v69, v69
	v_cvt_pk_bf16_f32 v66, v70, v66
	v_cvt_pk_bf16_f32 v67, v67, v68
	v_or_b32_e32 v70, 0x18100, v163
	v_pk_mul_f32 v[60:61], v[60:61], v[142:143] op_sel_hi:[1,0]
	v_max_f32_e32 v58, 0, v58
	v_cvt_pk_bf16_f32 v68, v74, v71
	v_cvt_pk_bf16_f32 v69, v72, v69
	global_store_dwordx4 v70, v[66:69], s[10:11] nt
	v_pk_mul_f32 v[64:65], v[64:65], v[142:143] op_sel_hi:[1,0]
	v_max_f32_e32 v59, 0, v59
	v_mul_f32_e32 v67, v58, v58
	v_max_f32_e32 v58, 0, v63
	v_max_f32_e32 v60, 0, v60
	v_max_f32_e32 v62, 0, v62
	v_mul_f32_e32 v58, v58, v58
	v_mul_f32_e32 v63, v59, v59
	v_max_f32_e32 v59, 0, v64
	v_mul_f32_e32 v64, v60, v60
	v_max_f32_e32 v60, 0, v65
	v_max_f32_e32 v61, 0, v61
	v_pk_mul_f32 v[50:51], v[50:51], v[142:143] op_sel_hi:[1,0]
	v_add_u32_e32 v66, 0x40000, v163
	v_mul_f32_e32 v62, v62, v62
	v_mul_f32_e32 v59, v59, v59
	v_mul_f32_e32 v60, v60, v60
	v_mul_f32_e32 v61, v61, v61
	v_cvt_pk_bf16_f32 v58, v62, v58
	v_pk_mul_f32 v[56:57], v[56:57], v[142:143] op_sel_hi:[1,0]
	v_pk_mul_f32 v[54:55], v[54:55], v[142:143] op_sel_hi:[1,0]
	v_pk_mul_f32 v[52:53], v[52:53], v[142:143] op_sel_hi:[1,0]
	v_max_f32_e32 v50, 0, v50
	v_max_f32_e32 v51, 0, v51
	v_cvt_pk_bf16_f32 v59, v59, v60
	v_cvt_pk_bf16_f32 v60, v67, v63
	v_cvt_pk_bf16_f32 v61, v64, v61
	global_store_dwordx4 v66, v[58:61], s[10:11]
	v_max_f32_e32 v54, 0, v54
	v_max_f32_e32 v52, 0, v52
	v_mul_f32_e32 v58, v50, v50
	v_max_f32_e32 v50, 0, v55
	v_mul_f32_e32 v55, v51, v51
	v_max_f32_e32 v51, 0, v56
	v_mul_f32_e32 v54, v54, v54
	v_mul_f32_e32 v50, v50, v50
	v_mul_f32_e32 v51, v51, v51
	v_mul_f32_e32 v56, v52, v52
	v_max_f32_e32 v52, 0, v57
	v_max_f32_e32 v53, 0, v53
	v_mul_f32_e32 v52, v52, v52
	v_mul_f32_e32 v53, v53, v53
	v_cvt_pk_bf16_f32 v50, v54, v50
	v_cvt_pk_bf16_f32 v51, v51, v52
	v_add_u32_e32 v54, 0x40100, v163
	v_cvt_pk_bf16_f32 v52, v58, v55
	v_cvt_pk_bf16_f32 v53, v56, v53
	global_store_dwordx4 v54, v[50:53], s[10:11]
	v_pk_mul_f32 v[26:27], v[26:27], v[140:141] op_sel_hi:[1,0]
	v_pk_mul_f32 v[30:31], v[30:31], v[140:141] op_sel_hi:[1,0]
	v_add_u32_e32 v51, 0x48000, v163
	v_mov_b32_e32 v50, v143
	v_pk_mul_f32 v[42:43], v[42:43], v[50:51] op_sel_hi:[1,0]
	v_pk_mul_f32 v[46:47], v[46:47], v[50:51] op_sel_hi:[1,0]
	v_pk_mul_f32 v[44:45], v[44:45], v[50:51] op_sel_hi:[1,0]
	v_max_f32_e32 v42, 0, v42
	v_pk_mul_f32 v[48:49], v[48:49], v[50:51] op_sel_hi:[1,0]
	v_mul_f32_e32 v52, v42, v42
	v_max_f32_e32 v42, 0, v47
	v_max_f32_e32 v43, 0, v43
	v_max_f32_e32 v44, 0, v44
	v_max_f32_e32 v46, 0, v46
	v_mul_f32_e32 v42, v42, v42
	v_mul_f32_e32 v47, v43, v43
; #define PG8_GAS __attribute__((address_space(1)))
; #define PG8_PACK8(y0, y1) (u32x4){cvt_pk_bf16((y0)[0], (y0)[1]), cvt_pk_bf16((y0)[2], (y0)[3]), cvt_pk_bf16((y1)[0], (y1)[1]), cvt_pk_bf16((y1)[2], (y1)[3])}
;     __device__ __forceinline__ void operator()(const f32x4 (&acc)[2][2][4][2], const Unit& u, int ui, int wr, int wc, int fr, int fq) const {
;     ...
;         for (int ai = 0; ai < 2; ++ai)
; #pragma unroll
;             for (int m = 0; m < 4; ++m) {
;                 const unsigned row = row0 + ai * HALF + m * 16; const float rs = rsv[ai][m];
; #pragma unroll
;                 for (int bj = 0; bj < 2; ++bj) {
;                     f32x4 y0 = acc[ai][bj][m][0] * rs, y1 = acc[ai][bj][m][1] * rs;
; #pragma unroll
;                     for (int e = 0; e < 4; ++e) { const float a = fmaxf(y0[e], 0.f), b = fmaxf(y1[e], 0.f); y0[e] = a * a; y1[e] = b * b; }
;                     const u32x4 hw = PG8_PACK8(y0, y1);
;     ...
;                     if (probe_mode == 1) { asm volatile("" :: "v"(hw)); } else
;     ...
;                     *(PG8_GAS u32x4*)((PG8_GAS unsigned char*)ws + E_QKVO + (size_t)((unsigned)(u.pm >> 4) * (24u << 20) + (unsigned)(u.pn >> 2) * (8u << 20) + row * 2048u + (colp + bj * HALF) * 2u)) = hw;
;                 }
	v_max_f32_e32 v43, 0, v48
	v_mul_f32_e32 v48, v44, v44
	v_max_f32_e32 v44, 0, v49
	v_max_f32_e32 v45, 0, v45
	v_pk_mul_f32 v[34:35], v[34:35], v[50:51] op_sel_hi:[1,0]
	v_mul_f32_e32 v46, v46, v46
	v_mul_f32_e32 v43, v43, v43
	v_mul_f32_e32 v44, v44, v44
	v_mul_f32_e32 v45, v45, v45
	v_cvt_pk_bf16_f32 v42, v46, v42
	v_pk_mul_f32 v[40:41], v[40:41], v[50:51] op_sel_hi:[1,0]
	v_pk_mul_f32 v[38:39], v[38:39], v[50:51] op_sel_hi:[1,0]
	v_pk_mul_f32 v[36:37], v[36:37], v[50:51] op_sel_hi:[1,0]
	v_max_f32_e32 v34, 0, v34
	v_max_f32_e32 v35, 0, v35
	v_cvt_pk_bf16_f32 v43, v43, v44
	v_cvt_pk_bf16_f32 v44, v52, v47
	v_cvt_pk_bf16_f32 v45, v48, v45
	global_store_dwordx4 v51, v[42:45], s[10:11]
	v_max_f32_e32 v38, 0, v38
	v_max_f32_e32 v36, 0, v36
	v_mul_f32_e32 v42, v34, v34
	v_max_f32_e32 v34, 0, v39
	v_mul_f32_e32 v39, v35, v35
	v_max_f32_e32 v35, 0, v40
	v_mul_f32_e32 v38, v38, v38
	v_mul_f32_e32 v34, v34, v34
	v_mul_f32_e32 v35, v35, v35
	v_mul_f32_e32 v40, v36, v36
	v_max_f32_e32 v36, 0, v41
	v_max_f32_e32 v37, 0, v37
	v_mul_f32_e32 v36, v36, v36
	v_mul_f32_e32 v37, v37, v37
	v_cvt_pk_bf16_f32 v34, v38, v34
	v_cvt_pk_bf16_f32 v35, v35, v36
	v_add_u32_e32 v38, 0x48100, v163
	v_pk_mul_f32 v[28:29], v[28:29], v[140:141] op_sel_hi:[1,0]
	v_max_f32_e32 v26, 0, v26
	v_cvt_pk_bf16_f32 v36, v42, v39
	v_cvt_pk_bf16_f32 v37, v40, v37
	global_store_dwordx4 v38, v[34:37], s[10:11]
	v_pk_mul_f32 v[32:33], v[32:33], v[140:141] op_sel_hi:[1,0]
	v_max_f32_e32 v27, 0, v27
	v_mul_f32_e32 v35, v26, v26
	v_max_f32_e32 v26, 0, v31
	v_max_f32_e32 v28, 0, v28
	v_max_f32_e32 v30, 0, v30
	v_mul_f32_e32 v26, v26, v26
	v_mul_f32_e32 v31, v27, v27
	v_max_f32_e32 v27, 0, v32
	v_mul_f32_e32 v32, v28, v28
	v_max_f32_e32 v28, 0, v33
	v_max_f32_e32 v29, 0, v29
	v_pk_mul_f32 v[18:19], v[18:19], v[140:141] op_sel_hi:[1,0]
	v_add_u32_e32 v34, 0x50000, v163
	v_mul_f32_e32 v30, v30, v30
	v_mul_f32_e32 v27, v27, v27
	v_mul_f32_e32 v28, v28, v28
	v_mul_f32_e32 v29, v29, v29
	v_cvt_pk_bf16_f32 v26, v30, v26
	v_pk_mul_f32 v[24:25], v[24:25], v[140:141] op_sel_hi:[1,0]
	v_pk_mul_f32 v[22:23], v[22:23], v[140:141] op_sel_hi:[1,0]
	v_pk_mul_f32 v[20:21], v[20:21], v[140:141] op_sel_hi:[1,0]
	v_max_f32_e32 v18, 0, v18
	v_max_f32_e32 v19, 0, v19
	v_cvt_pk_bf16_f32 v27, v27, v28
	v_cvt_pk_bf16_f32 v28, v35, v31
	v_cvt_pk_bf16_f32 v29, v32, v29
	global_store_dwordx4 v34, v[26:29], s[10:11]
	v_max_f32_e32 v22, 0, v22
	v_max_f32_e32 v20, 0, v20
	v_mul_f32_e32 v26, v18, v18
	v_max_f32_e32 v18, 0, v23
	v_mul_f32_e32 v23, v19, v19
	v_max_f32_e32 v19, 0, v24
	v_mul_f32_e32 v22, v22, v22
	v_mul_f32_e32 v18, v18, v18
	v_mul_f32_e32 v19, v19, v19
	v_mul_f32_e32 v24, v20, v20
	v_max_f32_e32 v20, 0, v25
	v_max_f32_e32 v21, 0, v21
	v_mul_f32_e32 v20, v20, v20
	v_mul_f32_e32 v21, v21, v21
	v_cvt_pk_bf16_f32 v18, v22, v18
	v_cvt_pk_bf16_f32 v19, v19, v20
	v_add_u32_e32 v22, 0x50100, v163
	v_cvt_pk_bf16_f32 v20, v26, v23
	v_cvt_pk_bf16_f32 v21, v24, v21
	global_store_dwordx4 v22, v[18:21], s[10:11]
	s_andn2_b64 vcc, exec, s[0:1]
	s_mov_b64 s[0:1], -1
	v_add_u32_e32 v19, 0x58000, v163
	v_mov_b32_e32 v18, v141
	v_pk_mul_f32 v[10:11], v[10:11], v[18:19] op_sel_hi:[1,0]
	v_pk_mul_f32 v[14:15], v[14:15], v[18:19] op_sel_hi:[1,0]
	v_pk_mul_f32 v[12:13], v[12:13], v[18:19] op_sel_hi:[1,0]
	v_max_f32_e32 v10, 0, v10
	v_pk_mul_f32 v[16:17], v[16:17], v[18:19] op_sel_hi:[1,0]
	v_mul_f32_e32 v20, v10, v10
	v_max_f32_e32 v10, 0, v15
	v_max_f32_e32 v11, 0, v11
	v_max_f32_e32 v12, 0, v12
	v_max_f32_e32 v14, 0, v14
	v_mul_f32_e32 v10, v10, v10
	v_mul_f32_e32 v15, v11, v11
	v_max_f32_e32 v11, 0, v16
	v_mul_f32_e32 v16, v12, v12
	v_max_f32_e32 v12, 0, v17
	v_max_f32_e32 v13, 0, v13
	v_pk_mul_f32 v[2:3], v[2:3], v[18:19] op_sel_hi:[1,0]
	v_mul_f32_e32 v14, v14, v14
	v_mul_f32_e32 v11, v11, v11
	v_mul_f32_e32 v12, v12, v12
	v_mul_f32_e32 v13, v13, v13
	v_cvt_pk_bf16_f32 v10, v14, v10
	v_pk_mul_f32 v[6:7], v[6:7], v[18:19] op_sel_hi:[1,0]
	v_pk_mul_f32 v[4:5], v[4:5], v[18:19] op_sel_hi:[1,0]
	v_max_f32_e32 v2, 0, v2
	v_cvt_pk_bf16_f32 v11, v11, v12
	v_cvt_pk_bf16_f32 v12, v20, v15
	v_cvt_pk_bf16_f32 v13, v16, v13
	global_store_dwordx4 v19, v[10:13], s[10:11]
	v_pk_mul_f32 v[8:9], v[8:9], v[18:19] op_sel_hi:[1,0]
	v_max_f32_e32 v6, 0, v6
	v_mul_f32_e32 v10, v2, v2
	v_max_f32_e32 v2, 0, v7
	v_max_f32_e32 v3, 0, v3
	v_max_f32_e32 v4, 0, v4
	v_mul_f32_e32 v6, v6, v6
	v_mul_f32_e32 v2, v2, v2
	v_mul_f32_e32 v7, v3, v3
	v_max_f32_e32 v3, 0, v8
	v_mul_f32_e32 v8, v4, v4
	v_max_f32_e32 v4, 0, v9
	v_max_f32_e32 v5, 0, v5
	v_mul_f32_e32 v3, v3, v3
	v_mul_f32_e32 v4, v4, v4
	v_mul_f32_e32 v5, v5, v5
	v_cvt_pk_bf16_f32 v2, v6, v2
	v_add_u32_e32 v6, 0x58100, v163
	v_cvt_pk_bf16_f32 v3, v3, v4
	v_cvt_pk_bf16_f32 v4, v10, v7
	v_cvt_pk_bf16_f32 v5, v8, v5
	global_store_dwordx4 v6, v[2:5], s[10:11]
	s_mov_b32 s100, 2
	s_cbranch_vccnz .LBB0_53
	s_andn2_b64 vcc, exec, s[6:7]
	s_cbranch_vccnz .LBB0_52
	s_barrier
	s_branch .LBB0_52
